# v50 + NSA half-step tails: hipcc's two-branch waitcnt selection before the workgroup barrier (7 scalar ops, taken branch) shortened to one wait, one test and a rare out-of-line vmcnt(0) stub (11 sites
# speedup vs baseline: 1.0052x; 1.0023x over previous
.LBB0_1725:
	v_cndmask_b32_e64 v0, 0, 1, s[14:15]
	v_cmp_ne_u32_e64 s[12:13], 1, v0
	s_waitcnt vmcnt(2) lgkmcnt(0)
	s_andn2_b64 vcc, exec, s[14:15]
	s_cbranch_vccnz .Lwz10

.LBB0_1737:
	s_waitcnt vmcnt(2) lgkmcnt(0)
	s_and_b64 vcc, exec, s[12:13]
	s_cbranch_vccnz .Lwz9

.LBB0_1749:
	s_waitcnt vmcnt(2) lgkmcnt(0)
	s_andn2_b64 vcc, exec, s[14:15]
	s_cbranch_vccnz .Lwz8

.LBB0_1777:
	v_cndmask_b32_e64 v1, 0, 1, s[18:19]
	v_cmp_ne_u32_e64 s[14:15], 1, v1
	s_waitcnt vmcnt(2) lgkmcnt(0)
	s_andn2_b64 vcc, exec, s[18:19]
	s_cbranch_vccnz .Lwz7

.LBB0_1789:
	s_waitcnt vmcnt(2) lgkmcnt(0)
	s_and_b64 vcc, exec, s[14:15]
	s_cbranch_vccnz .Lwz6

.LBB0_1832:
	v_cndmask_b32_e64 v1, 0, 1, s[14:15]
	v_cmp_ne_u32_e64 s[10:11], 1, v1
	s_waitcnt vmcnt(2) lgkmcnt(0)
	s_andn2_b64 vcc, exec, s[14:15]
	s_cbranch_vccnz .Lwz5

.LBB0_1844:
	s_waitcnt vmcnt(2) lgkmcnt(0)
	s_and_b64 vcc, exec, s[10:11]
	s_cbranch_vccnz .Lwz4

.LBB0_2024:
	v_cndmask_b32_e64 v1, 0, 1, s[78:79]
	v_cmp_ne_u32_e64 s[8:9], 1, v1
	s_waitcnt vmcnt(2) lgkmcnt(0)
	s_andn2_b64 vcc, exec, s[78:79]
	s_cbranch_vccnz .Lwz1

.Lwz0:
	s_waitcnt vmcnt(0)
	s_branch .Lwz0_b
